# v23 + one extra un-waited L2 writeback per XCD and grid barrier, issued by the 16th arriver, to start flushing dirty lines while the rest still arrive
# speedup vs baseline: 1.0021x; 1.0021x over previous
.LBB0_87:
	s_or_b64 exec, exec, s[28:29]
	v_cvt_f32_u32_e32 v5, v3
	s_waitcnt vmcnt(0)
	buffer_inv sc1
	v_readfirstlane_b32 s4, v4
	s_and_b32 s100, s4, 31
	s_cmp_lg_u32 s100, 15
	s_cbranch_scc1 .Lmidwb_7
	buffer_wbl2 sc1
.Lmidwb_7:
	v_sub_u32_e32 v4, 0, v3
	v_rcp_iflag_f32_e32 v5, v5
	v_add_u32_e32 v6, s4, v1
	v_mul_f32_e32 v5, 0x4f7ffffe, v5
	v_cvt_u32_f32_e32 v5, v5
	v_mul_lo_u32 v1, v4, v5
	v_mul_hi_u32 v1, v5, v1
	v_add_u32_e32 v1, v5, v1
	v_mul_hi_u32 v1, v6, v1
	v_mul_lo_u32 v4, v1, v3
	v_sub_u32_e32 v4, v6, v4
	v_add_u32_e32 v5, 1, v1
	v_cmp_ge_u32_e32 vcc, v4, v3
	s_nop 1
	v_cndmask_b32_e32 v1, v1, v5, vcc
	v_sub_u32_e32 v5, v4, v3
	v_cndmask_b32_e32 v4, v4, v5, vcc
	v_add_u32_e32 v5, 1, v1
	v_cmp_ge_u32_e32 vcc, v4, v3
	v_add_u32_e32 v4, 1, v6
	s_nop 0
	v_cndmask_b32_e32 v1, v1, v5, vcc
	v_mul_lo_u32 v5, v3, v1
	v_add_u32_e32 v3, v5, v3
	v_cmp_ne_u32_e32 vcc, v4, v3
	s_and_saveexec_b64 s[4:5], vcc
	s_xor_b64 s[28:29], exec, s[4:5]
	s_cbranch_execz .LBB0_101
	v_readlane_b32 s4, v254, 45
	v_readlane_b32 s5, v254, 46
	s_waitcnt lgkmcnt(0)
	s_nop 3
	global_load_dword v2, v115, s[4:5] sc1
	s_waitcnt vmcnt(0)
	v_cmp_eq_u32_e32 vcc, v2, v1
	s_and_saveexec_b64 s[38:39], vcc
	s_cbranch_execz .LBB0_100
	s_mov_b32 s4, 1
	s_mov_b64 s[40:41], 0
	s_branch .LBB0_91

.LBB0_238:
	s_or_b64 exec, exec, s[26:27]
	v_cvt_f32_u32_e32 v5, v3
	s_waitcnt vmcnt(0)
	buffer_inv sc1
	v_readfirstlane_b32 s4, v4
	s_and_b32 s100, s4, 31
	s_cmp_lg_u32 s100, 15
	s_cbranch_scc1 .Lmidwb_6
	buffer_wbl2 sc1
.Lmidwb_6:
	v_sub_u32_e32 v4, 0, v3
	v_rcp_iflag_f32_e32 v5, v5
	v_add_u32_e32 v6, s4, v1
	v_mul_f32_e32 v5, 0x4f7ffffe, v5
	v_cvt_u32_f32_e32 v5, v5
	v_mul_lo_u32 v1, v4, v5
	v_mul_hi_u32 v1, v5, v1
	v_add_u32_e32 v1, v5, v1
	v_mul_hi_u32 v1, v6, v1
	v_mul_lo_u32 v4, v1, v3
	v_sub_u32_e32 v4, v6, v4
	v_add_u32_e32 v5, 1, v1
	v_cmp_ge_u32_e32 vcc, v4, v3
	s_nop 1
	v_cndmask_b32_e32 v1, v1, v5, vcc
	v_sub_u32_e32 v5, v4, v3
	v_cndmask_b32_e32 v4, v4, v5, vcc
	v_add_u32_e32 v5, 1, v1
	v_cmp_ge_u32_e32 vcc, v4, v3
	v_add_u32_e32 v4, 1, v6
	s_nop 0
	v_cndmask_b32_e32 v1, v1, v5, vcc
	v_mul_lo_u32 v5, v3, v1
	v_add_u32_e32 v3, v5, v3
	v_cmp_ne_u32_e32 vcc, v4, v3
	s_and_saveexec_b64 s[4:5], vcc
	s_xor_b64 s[26:27], exec, s[4:5]
	s_cbranch_execz .LBB0_252
	v_readlane_b32 s4, v254, 45
	v_readlane_b32 s5, v254, 46
	s_waitcnt lgkmcnt(0)
	s_nop 3
	global_load_dword v2, v115, s[4:5] sc1
	s_waitcnt vmcnt(0)
	v_cmp_eq_u32_e32 vcc, v2, v1
	s_and_saveexec_b64 s[28:29], vcc
	s_cbranch_execz .LBB0_251
	s_mov_b32 s4, 1
	s_mov_b64 s[38:39], 0
	s_branch .LBB0_242

.LBB0_413:
	s_or_b64 exec, exec, s[10:11]
	v_cvt_f32_u32_e32 v5, v3
	s_waitcnt vmcnt(0)
	buffer_inv sc1
	v_readfirstlane_b32 s4, v4
	s_and_b32 s100, s4, 31
	s_cmp_lg_u32 s100, 15
	s_cbranch_scc1 .Lmidwb_5
	buffer_wbl2 sc1
.Lmidwb_5:
	v_sub_u32_e32 v4, 0, v3
	v_rcp_iflag_f32_e32 v5, v5
	v_add_u32_e32 v6, s4, v1
	v_mul_f32_e32 v5, 0x4f7ffffe, v5
	v_cvt_u32_f32_e32 v5, v5
	v_mul_lo_u32 v1, v4, v5
	v_mul_hi_u32 v1, v5, v1
	v_add_u32_e32 v1, v5, v1
	v_mul_hi_u32 v1, v6, v1
	v_mul_lo_u32 v4, v1, v3
	v_sub_u32_e32 v4, v6, v4
	v_add_u32_e32 v5, 1, v1
	v_cmp_ge_u32_e32 vcc, v4, v3
	s_nop 1
	v_cndmask_b32_e32 v1, v1, v5, vcc
	v_sub_u32_e32 v5, v4, v3
	v_cndmask_b32_e32 v4, v4, v5, vcc
	v_add_u32_e32 v5, 1, v1
	v_cmp_ge_u32_e32 vcc, v4, v3
	v_add_u32_e32 v4, 1, v6
	s_nop 0
	v_cndmask_b32_e32 v1, v1, v5, vcc
	v_mul_lo_u32 v5, v3, v1
	v_add_u32_e32 v3, v5, v3
	v_cmp_ne_u32_e32 vcc, v4, v3
	s_and_saveexec_b64 s[4:5], vcc
	s_xor_b64 s[10:11], exec, s[4:5]
	s_cbranch_execz .LBB0_427
	v_readlane_b32 s4, v254, 45
	v_readlane_b32 s5, v254, 46
	s_waitcnt lgkmcnt(0)
	s_nop 3
	global_load_dword v2, v115, s[4:5] sc1
	s_waitcnt vmcnt(0)
	v_cmp_eq_u32_e32 vcc, v2, v1
	s_and_saveexec_b64 s[26:27], vcc
	s_cbranch_execz .LBB0_426
	s_mov_b32 s4, 1
	s_mov_b64 s[28:29], 0
	s_branch .LBB0_417

.Lmidwb_4:
	v_sub_u32_e32 v4, 0, v3
	v_rcp_iflag_f32_e32 v5, v5
	v_add_u32_e32 v6, s4, v1
	v_mul_f32_e32 v5, 0x4f7ffffe, v5
	v_cvt_u32_f32_e32 v5, v5
	v_mul_lo_u32 v1, v4, v5
	v_mul_hi_u32 v1, v5, v1
	v_add_u32_e32 v1, v5, v1
	v_mul_hi_u32 v1, v6, v1
	v_mul_lo_u32 v4, v1, v3
	v_sub_u32_e32 v4, v6, v4
	v_add_u32_e32 v5, 1, v1
	v_cmp_ge_u32_e32 vcc, v4, v3
	s_nop 1
	v_cndmask_b32_e32 v1, v1, v5, vcc
	v_sub_u32_e32 v5, v4, v3
	v_cndmask_b32_e32 v4, v4, v5, vcc
	v_add_u32_e32 v5, 1, v1
	v_cmp_ge_u32_e32 vcc, v4, v3
	v_add_u32_e32 v4, 1, v6
	s_nop 0
	v_cndmask_b32_e32 v1, v1, v5, vcc
	v_mul_lo_u32 v5, v3, v1
	v_add_u32_e32 v3, v5, v3
	v_cmp_ne_u32_e32 vcc, v4, v3
	s_and_saveexec_b64 s[4:5], vcc
	s_xor_b64 s[10:11], exec, s[4:5]
	s_cbranch_execz .LBB0_583
	v_readlane_b32 s4, v254, 45
	v_readlane_b32 s5, v254, 46
	s_waitcnt lgkmcnt(0)
	s_nop 3
	global_load_dword v2, v115, s[4:5] sc1
	s_waitcnt vmcnt(0)
	v_cmp_eq_u32_e32 vcc, v2, v1
	s_and_saveexec_b64 s[28:29], vcc
	s_cbranch_execz .LBB0_582
	s_mov_b32 s4, 1
	s_mov_b64 s[38:39], 0
	s_branch .LBB0_573

.LBB0_1021:
	s_or_b64 exec, exec, s[4:5]
	v_cvt_f32_u32_e32 v5, v3
	s_waitcnt vmcnt(0)
	buffer_inv sc1
	v_readfirstlane_b32 s4, v4
	s_and_b32 s100, s4, 31
	s_cmp_lg_u32 s100, 15
	s_cbranch_scc1 .Lmidwb_2
	buffer_wbl2 sc1
.Lmidwb_2:
	v_sub_u32_e32 v4, 0, v3
	v_rcp_iflag_f32_e32 v5, v5
	v_add_u32_e32 v6, s4, v1
	v_mul_f32_e32 v5, 0x4f7ffffe, v5
	v_cvt_u32_f32_e32 v5, v5
	v_mul_lo_u32 v1, v4, v5
	v_mul_hi_u32 v1, v5, v1
	v_add_u32_e32 v1, v5, v1
	v_mul_hi_u32 v1, v6, v1
	v_mul_lo_u32 v4, v1, v3
	v_sub_u32_e32 v4, v6, v4
	v_add_u32_e32 v5, 1, v1
	v_cmp_ge_u32_e32 vcc, v4, v3
	s_nop 1
	v_cndmask_b32_e32 v1, v1, v5, vcc
	v_sub_u32_e32 v5, v4, v3
	v_cndmask_b32_e32 v4, v4, v5, vcc
	v_add_u32_e32 v5, 1, v1
	v_cmp_ge_u32_e32 vcc, v4, v3
	v_add_u32_e32 v4, 1, v6
	s_nop 0
	v_cndmask_b32_e32 v1, v1, v5, vcc
	v_mul_lo_u32 v5, v3, v1
	v_add_u32_e32 v3, v5, v3
	v_cmp_ne_u32_e32 vcc, v4, v3
	s_and_saveexec_b64 s[4:5], vcc
	s_xor_b64 s[4:5], exec, s[4:5]
	s_cbranch_execz .LBB0_1035
	v_readlane_b32 s8, v254, 45
	v_readlane_b32 s9, v254, 46
	s_waitcnt lgkmcnt(0)
	s_nop 3
	global_load_dword v2, v115, s[8:9] sc1
	s_waitcnt vmcnt(0)
	v_cmp_eq_u32_e32 vcc, v2, v1
	s_and_saveexec_b64 s[8:9], vcc
	s_cbranch_execz .LBB0_1034
	s_mov_b32 s7, 1
	s_mov_b64 s[10:11], 0
	s_branch .LBB0_1025

.LBB0_1124:
	s_or_b64 exec, exec, s[8:9]
	v_cvt_f32_u32_e32 v5, v3
	s_waitcnt vmcnt(0)
	buffer_inv sc1
	v_readfirstlane_b32 s7, v4
	s_and_b32 s100, s7, 31
	s_cmp_lg_u32 s100, 15
	s_cbranch_scc1 .Lmidwb_1
	buffer_wbl2 sc1
.Lmidwb_1:
	v_sub_u32_e32 v4, 0, v3
	v_rcp_iflag_f32_e32 v5, v5
	v_add_u32_e32 v6, s7, v1
	v_mul_f32_e32 v5, 0x4f7ffffe, v5
	v_cvt_u32_f32_e32 v5, v5
	v_mul_lo_u32 v1, v4, v5
	v_mul_hi_u32 v1, v5, v1
	v_add_u32_e32 v1, v5, v1
	v_mul_hi_u32 v1, v6, v1
	v_mul_lo_u32 v4, v1, v3
	v_sub_u32_e32 v4, v6, v4
	v_add_u32_e32 v5, 1, v1
	v_cmp_ge_u32_e32 vcc, v4, v3
	s_nop 1
	v_cndmask_b32_e32 v1, v1, v5, vcc
	v_sub_u32_e32 v5, v4, v3
	v_cndmask_b32_e32 v4, v4, v5, vcc
	v_add_u32_e32 v5, 1, v1
	v_cmp_ge_u32_e32 vcc, v4, v3
	v_add_u32_e32 v4, 1, v6
	s_nop 0
	v_cndmask_b32_e32 v1, v1, v5, vcc
	v_mul_lo_u32 v5, v3, v1
	v_add_u32_e32 v3, v5, v3
	v_cmp_ne_u32_e32 vcc, v4, v3
	s_and_saveexec_b64 s[8:9], vcc
	s_xor_b64 s[8:9], exec, s[8:9]
	s_cbranch_execz .LBB0_1138
	v_readlane_b32 s10, v254, 45
	v_readlane_b32 s11, v254, 46
	s_waitcnt lgkmcnt(0)
	s_nop 3
	global_load_dword v2, v115, s[10:11] sc1
	s_waitcnt vmcnt(0)
	v_cmp_eq_u32_e32 vcc, v2, v1
	s_and_saveexec_b64 s[10:11], vcc
	s_cbranch_execz .LBB0_1137
	s_mov_b32 s7, 1
	s_mov_b64 s[26:27], 0
	s_branch .LBB0_1128
